# speedup vs baseline: 1.0171x; 1.0171x over previous
_ZN12_GLOBAL__N_113search_kernelEPKfS1_PhPf:
	s_load_dwordx2 s[8:9], s[0:1], 0x0
	s_load_dwordx2 s[4:5], s[0:1], 0x10
	s_movk_i32 s3, 0x90
	v_readfirstlane_b32 s10, v0
	v_cmp_gt_u32_e32 vcc, s3, v0
	s_and_saveexec_b64 s[6:7], vcc
	v_mov_b32_e32 v2, -1
	v_lshlrev_b32_e32 v1, 3, v0
	v_mov_b32_e32 v3, v2
	ds_write_b64 v1, v[2:3] offset:16384
	s_or_b64 exec, exec, s[6:7]
	s_waitcnt lgkmcnt(0)
	s_add_u32 s6, s4, 0x240000
	s_addc_u32 s7, s5, 0
	s_lshl_b32 s11, s2, 1
	s_and_b32 s14, s11, 14
	s_ashr_i32 s11, s2, 7
	s_lshr_b32 s15, s10, 6
	s_add_i32 s14, s14, s11
	s_bfe_u32 s2, s2, 0x40003
	s_mul_i32 s11, s15, 24
	v_mul_u32_u24_e32 v2, 0x71d, v0
	v_mul_u32_u24_e32 v4, 0x195, v0
	s_min_u32 s18, s11, 0xa5
	s_mul_i32 s11, s14, 3
	s_mul_i32 s12, s2, 9
	s_mov_b32 s13, 0
	v_lshrrev_b32_e32 v3, 16, v2
	s_movk_i32 s19, 0xffdc
	v_lshrrev_b32_e32 v5, 17, v4
	v_mad_i32_i24 v2, v3, s19, v0
	v_mad_i32_i24 v4, v5, -9, v3
	v_add_u32_e32 v3, s11, v5
	v_mov_b64_e32 v[6:7], s[12:13]
	v_mad_i64_i32 v[8:9], s[16:17], v3, s3, v[6:7]
	v_ashrrev_i32_e32 v5, 31, v4
	v_lshl_add_u64 v[4:5], v[8:9], 0, v[4:5]
	s_movk_i32 s13, 0x240
	v_mov_b64_e32 v[8:9], s[8:9]
	v_mad_u64_u32 v[10:11], s[8:9], v4, s13, v[8:9]
	v_min_u32_e32 v4, 0x1cb, v0
	v_or_b32_e32 v4, 0x200, v4
	v_mad_i32_i24 v11, v5, s13, v11
	v_mul_u32_u24_e32 v5, 0x71d, v4
	v_ashrrev_i32_e32 v3, 31, v2
	v_lshrrev_b32_e32 v5, 16, v5
	v_lshl_add_u64 v[2:3], v[2:3], 4, v[10:11]
	v_mad_i32_i24 v10, v5, s19, v4
	v_mul_u32_u24_e32 v4, 0x653, v4
	v_lshrrev_b32_e32 v11, 19, v4
	v_mad_i32_i24 v4, v11, -9, v5
	v_add_u32_e32 v5, s11, v11
	v_mad_i64_i32 v[6:7], s[8:9], v5, s3, v[6:7]
	v_ashrrev_i32_e32 v5, 31, v4
	v_lshl_add_u64 v[4:5], v[6:7], 0, v[4:5]
	v_mad_u64_u32 v[12:13], s[8:9], v4, s13, v[8:9]
	s_mul_i32 s8, s14, 0x90
	s_barrier
	s_load_dwordx2 s[42:43], s[0:1], 0x8
	v_mov_b32_e32 v16, 0
	v_mov_b32_e32 v17, 0
	ds_write_b64 v16, v[16:17] offset:18112
	s_load_dwordx2 s[62:63], s[0:1], 0x0
	v_mov_b32_e32 v244, v2
	v_mov_b32_e32 v245, v3
	global_load_dwordx4 v[6:9], v[2:3], off
	v_mad_i32_i24 v13, v5, s13, v13
	v_ashrrev_i32_e32 v11, 31, v10
	v_lshl_add_u64 v[10:11], v[10:11], 4, v[12:13]
	v_mov_b32_e32 v246, v10
	v_mov_b32_e32 v247, v11
	global_load_dwordx4 v[10:13], v[10:11], off
	v_and_b32_e32 v1, 63, v0
	s_add_i32 s20, s8, s12
	s_lshl_b32 s20, s20, 10
	v_lshl_add_u32 v164, v1, 4, s20
	s_mul_i32 s9, s14, 0xbd
	s_add_i32 s21, s9, s18
	s_lshl_b32 s21, s21, 10
	v_lshl_add_u32 v165, v1, 4, s21
	s_add_u32 s22, s4, 0x1000
	s_addc_u32 s23, s5, 0
	s_add_u32 s24, s4, 0x2000
	s_addc_u32 s25, s5, 0
	s_mov_b32 s26, s6
	s_mov_b32 s27, s7
	s_add_u32 s28, s6, 0x1000
	s_addc_u32 s29, s7, 0
	s_add_u32 s30, s6, 0x2000
	s_addc_u32 s31, s7, 0
	s_add_u32 s32, s6, 0x3000
	s_addc_u32 s33, s7, 0
	s_add_u32 s34, s6, 0x4000
	s_addc_u32 s35, s7, 0
	s_add_u32 s36, s6, 0x5000
	s_addc_u32 s37, s7, 0
	v_bfe_u32 v166, v0, 4, 2
	v_and_b32_e32 v167, 15, v0
	v_lshlrev_b32_e32 v167, 3, v167
	s_mul_i32 s40, s15, 6
	s_mov_b32 s41, 0x7f000000
	global_load_dwordx4 v[112:115], v164, s[4:5]
	global_load_dwordx4 v[16:19], v165, s[26:27] nt
	global_load_dwordx4 v[20:23], v165, s[26:27] offset:1024 nt
	global_load_dwordx4 v[24:27], v165, s[26:27] offset:2048 nt
	global_load_dwordx4 v[28:31], v165, s[26:27] offset:3072 nt
	global_load_dwordx4 v[32:35], v165, s[28:29] nt
	global_load_dwordx4 v[36:39], v165, s[28:29] offset:1024 nt
	global_load_dwordx4 v[40:43], v165, s[28:29] offset:2048 nt
	global_load_dwordx4 v[44:47], v165, s[28:29] offset:3072 nt
	global_load_dwordx4 v[48:51], v165, s[30:31] nt
	global_load_dwordx4 v[52:55], v165, s[30:31] offset:1024 nt
	global_load_dwordx4 v[56:59], v165, s[30:31] offset:2048 nt
	global_load_dwordx4 v[60:63], v165, s[30:31] offset:3072 nt
	global_load_dwordx4 v[64:67], v165, s[32:33] nt
	global_load_dwordx4 v[68:71], v165, s[32:33] offset:1024 nt
	global_load_dwordx4 v[72:75], v165, s[32:33] offset:2048 nt
	global_load_dwordx4 v[76:79], v165, s[32:33] offset:3072 nt
	global_load_dwordx4 v[80:83], v165, s[34:35] nt
	global_load_dwordx4 v[84:87], v165, s[34:35] offset:1024 nt
	global_load_dwordx4 v[88:91], v165, s[34:35] offset:2048 nt
	global_load_dwordx4 v[92:95], v165, s[34:35] offset:3072 nt
	global_load_dwordx4 v[96:99], v165, s[36:37] nt
	global_load_dwordx4 v[100:103], v165, s[36:37] offset:1024 nt
	global_load_dwordx4 v[104:107], v165, s[36:37] offset:2048 nt
	global_load_dwordx4 v[108:111], v165, s[36:37] offset:3072 nt
	global_load_dwordx4 v[116:119], v164, s[4:5] offset:1024
	v_lshlrev_b32_e32 v14, 4, v0
	s_lshr_b32 s50, s15, 1
	s_and_b32 s51, s15, 1
	s_lshl_b32 s51, s51, 3
	s_mov_b32 s48, 0x1010101
	s_mov_b32 s49, 0x1010101
	s_movk_i32 s58, 0x900
	s_movk_i32 s59, 0xb40
	v_and_b32_e32 v168, 7, v0
	v_lshrrev_b32_e32 v177, 3, v1
	v_or_b32_e32 v177, s51, v177
	v_lshlrev_b32_e32 v169, 3, v177
	v_and_b32_e32 v179, 3, v0
	v_lshlrev_b32_e32 v179, 8, v179
	v_lshl_add_u32 v170, v177, 4, v179
	v_add_u32_e32 v170, s20, v170
	v_lshrrev_b32_e32 v179, 2, v168
	v_and_b32_e32 v180, 3, v0
	v_lshl_or_b32 v171, v179, 4, v180
	v_mul_u32_u24_e32 v179, 11, v168
	v_lshrrev_b32_e32 v179, 5, v179
	v_mul_u32_u24_e32 v180, 3, v179
	v_sub_u32_e32 v180, v168, v180
	v_mul_u32_u24_e32 v181, 0x90, v179
	v_add_u32_e32 v181, v181, v180
	v_mul_u32_u24_e32 v172, 0x240, v181
	v_mul_u32_u24_e32 v181, 0x48, v179
	v_add_u32_e32 v181, v181, v180
	v_mul_u32_u24_e32 v173, 0x120, v181
	v_mul_u32_u24_e32 v181, 0x24, v179
	v_add_u32_e32 v181, v181, v180
	v_mul_u32_u24_e32 v174, 0x90, v181
	v_mul_u32_u24_e32 v181, 9, v179
	v_add_u32_e32 v181, v181, v180
	v_mul_u32_u24_e32 v175, 0x240, v181
	v_add_u32_e32 v176, 8, v168
	s_waitcnt lgkmcnt(0)
	s_mul_i32 s60, s14, 0x3cc00
	s_add_u32 s42, s42, s60
	s_addc_u32 s43, s43, 0
	s_mul_i32 s60, s14, 0xf300
	s_add_u32 s44, s4, s60
	s_addc_u32 s45, s5, 0
	s_add_u32 s44, s44, 0x534000
	s_addc_u32 s45, s45, 0
	s_mul_i32 s60, s14, 0x3cc0
	s_add_u32 s46, s4, s60
	s_addc_u32 s47, s5, 0
	s_add_u32 s46, s46, 0x627000
	s_addc_u32 s47, s47, 0
	v_mov_b32_e32 v152, s42
	v_mov_b32_e32 v153, s43
	v_mov_b32_e32 v154, s44
	v_mov_b32_e32 v155, s45
	v_mov_b32_e32 v159, s46
	v_mov_b32_e32 v161, s47
	s_sub_u32 s60, s42, s62
	s_subb_u32 s61, s43, s63
	s_mul_i32 s62, s14, 0x3cc00
	s_sub_u32 s60, s60, s62
	s_subb_u32 s61, s61, 0
	v_lshl_add_u64 v[244:245], v[244:245], 0, s[60:61]
	v_lshl_add_u64 v[246:247], v[246:247], 0, s[60:61]
	s_lshl_b32 s62, s15, 10
	s_add_i32 s62, s62, 0x46e0
	s_mov_b32 m0, s62
	s_mul_i32 s62, s2, 0xf30
	s_add_u32 s60, s44, s62
	s_addc_u32 s61, s45, 0
	v_lshlrev_b32_e32 v240, 4, v0
	v_mov_b32_e32 v241, 0
	v_lshl_add_u64 v[240:241], v[240:241], 0, s[60:61]
	s_mul_i32 s62, s2, 0x3cc
	s_add_u32 s60, s46, s62
	s_addc_u32 s61, s47, 0
	v_lshlrev_b32_e32 v242, 2, v0
	v_mov_b32_e32 v243, 0
	v_lshl_add_u64 v[242:243], v[242:243], 0, s[60:61]
	s_load_dwordx2 s[2:3], s[0:1], 0x18
	s_waitcnt vmcnt(21)
	ds_write_b128 v14, v[6:9]
	ds_write_b128 v14, v[10:13] offset:8192
	v_mfma_f32_16x16x32_f16 v[120:123], v[16:19], v[112:115], 0
	v_mfma_f32_16x16x32_f16 v[124:127], v[20:23], v[112:115], 0
	v_mfma_f32_16x16x32_f16 v[128:131], v[24:27], v[112:115], 0
	v_mfma_f32_16x16x32_f16 v[132:135], v[28:31], v[112:115], 0
	s_waitcnt vmcnt(17)
	v_mfma_f32_16x16x32_f16 v[136:139], v[32:35], v[112:115], 0
	v_mfma_f32_16x16x32_f16 v[140:143], v[36:39], v[112:115], 0
	v_mfma_f32_16x16x32_f16 v[144:147], v[40:43], v[112:115], 0
	v_mfma_f32_16x16x32_f16 v[148:151], v[44:47], v[112:115], 0
	v_min3_i32 v160, v120, v121, s41
	v_min3_i32 v160, v122, v123, v160
	v_min3_i32 v160, v124, v125, v160
	v_min3_i32 v160, v126, v127, v160
	v_min3_i32 v160, v128, v129, v160
	v_min3_i32 v160, v130, v131, v160
	v_min3_i32 v160, v132, v133, v160
	v_min3_i32 v157, v134, v135, v160
	v_mov_b32_e32 v6, 0
	v_mov_b32_e32 v7, 0x900
	v_mov_b32_e32 v8, 0x240
	s_waitcnt vmcnt(13)
	v_mfma_f32_16x16x32_f16 v[120:123], v[48:51], v[112:115], 0
	v_mfma_f32_16x16x32_f16 v[124:127], v[52:55], v[112:115], 0
	v_mov_b32_e32 v158, 0
	v_mfma_f32_16x16x32_f16 v[128:131], v[56:59], v[112:115], 0
	v_mfma_f32_16x16x32_f16 v[132:135], v[60:63], v[112:115], 0
	v_min3_i32 v160, v136, v137, v157
	v_min3_i32 v160, v138, v139, v160
	v_min3_i32 v160, v140, v141, v160
	v_min3_i32 v160, v142, v143, v160
	v_min3_i32 v160, v144, v145, v160
	v_min3_i32 v160, v146, v147, v160
	v_min3_i32 v160, v148, v149, v160
	v_min3_i32 v156, v150, v151, v160
	v_cmp_ge_i32_e32 vcc, v156, v157
	s_waitcnt vmcnt(9)
	v_mfma_f32_16x16x32_f16 v[136:139], v[64:67], v[112:115], 0
	v_mfma_f32_16x16x32_f16 v[140:143], v[68:71], v[112:115], 0
	v_cndmask_b32_e32 v158, 1, v158, vcc
	v_mfma_f32_16x16x32_f16 v[144:147], v[72:75], v[112:115], 0
	v_mfma_f32_16x16x32_f16 v[148:151], v[76:79], v[112:115], 0
	v_min3_i32 v160, v120, v121, v156
	v_min3_i32 v160, v122, v123, v160
	v_min3_i32 v160, v124, v125, v160
	v_min3_i32 v160, v126, v127, v160
	v_min3_i32 v160, v128, v129, v160
	v_min3_i32 v160, v130, v131, v160
	v_min3_i32 v160, v132, v133, v160
	v_min3_i32 v157, v134, v135, v160
	v_cmp_ge_i32_e32 vcc, v157, v156
	s_waitcnt vmcnt(5)
	v_mfma_f32_16x16x32_f16 v[120:123], v[80:83], v[112:115], 0
	v_mfma_f32_16x16x32_f16 v[124:127], v[84:87], v[112:115], 0
	v_cndmask_b32_e32 v158, 2, v158, vcc
	v_mfma_f32_16x16x32_f16 v[128:131], v[88:91], v[112:115], 0
	v_mfma_f32_16x16x32_f16 v[132:135], v[92:95], v[112:115], 0
	v_min3_i32 v160, v136, v137, v157
	v_min3_i32 v160, v138, v139, v160
	v_min3_i32 v160, v140, v141, v160
	v_min3_i32 v160, v142, v143, v160
	v_min3_i32 v160, v144, v145, v160
	v_min3_i32 v160, v146, v147, v160
	v_min3_i32 v160, v148, v149, v160
	v_min3_i32 v156, v150, v151, v160
	v_cmp_ge_i32_e32 vcc, v156, v157
	s_waitcnt vmcnt(1)
	v_mfma_f32_16x16x32_f16 v[136:139], v[96:99], v[112:115], 0
	v_mfma_f32_16x16x32_f16 v[140:143], v[100:103], v[112:115], 0
	v_cndmask_b32_e32 v158, 3, v158, vcc
	v_mfma_f32_16x16x32_f16 v[144:147], v[104:107], v[112:115], 0
	v_mfma_f32_16x16x32_f16 v[148:151], v[108:111], v[112:115], 0
	v_min3_i32 v160, v120, v121, v156
	v_min3_i32 v160, v122, v123, v160
	v_min3_i32 v160, v124, v125, v160
	v_min3_i32 v160, v126, v127, v160
	v_min3_i32 v160, v128, v129, v160
	v_min3_i32 v160, v130, v131, v160
	v_min3_i32 v160, v132, v133, v160
	v_min3_i32 v157, v134, v135, v160
	v_cmp_ge_i32_e32 vcc, v157, v156
	s_waitcnt vmcnt(0)
	global_load_dwordx4 v[112:115], v164, s[4:5] offset:2048
	v_mfma_f32_16x16x32_f16 v[120:123], v[16:19], v[116:119], 0
	v_mfma_f32_16x16x32_f16 v[124:127], v[20:23], v[116:119], 0
	v_cndmask_b32_e32 v158, 4, v158, vcc
	v_mfma_f32_16x16x32_f16 v[128:131], v[24:27], v[116:119], 0
	v_mfma_f32_16x16x32_f16 v[132:135], v[28:31], v[116:119], 0
	v_min3_i32 v160, v136, v137, v157
	v_min3_i32 v160, v138, v139, v160
	v_min3_i32 v160, v140, v141, v160
	v_min3_i32 v160, v142, v143, v160
	v_min3_i32 v160, v144, v145, v160
	v_min3_i32 v160, v146, v147, v160
	v_min3_i32 v160, v148, v149, v160
	v_min3_i32 v156, v150, v151, v160
	v_cmp_ge_i32_e32 vcc, v156, v157
	v_mfma_f32_16x16x32_f16 v[136:139], v[32:35], v[116:119], 0
	v_mfma_f32_16x16x32_f16 v[140:143], v[36:39], v[116:119], 0
	v_cndmask_b32_e32 v158, 5, v158, vcc
	v_add_u32_e32 v162, s40, v158
	v_lshl_or_b32 v162, v162, 2, v166
	v_mov_b32_e32 v163, v156
	ds_min_u64 v167, v[162:163] offset:16384
	v_mfma_f32_16x16x32_f16 v[144:147], v[40:43], v[116:119], 0
	v_mfma_f32_16x16x32_f16 v[148:151], v[44:47], v[116:119], 0
	v_min3_i32 v160, v120, v121, s41
	v_min3_i32 v160, v122, v123, v160
	v_min3_i32 v160, v124, v125, v160
	v_min3_i32 v160, v126, v127, v160
	v_min3_i32 v160, v128, v129, v160
	v_min3_i32 v160, v130, v131, v160
	v_min3_i32 v160, v132, v133, v160
	v_min3_i32 v157, v134, v135, v160
	v_mfma_f32_16x16x32_f16 v[120:123], v[48:51], v[116:119], 0
	v_mfma_f32_16x16x32_f16 v[124:127], v[52:55], v[116:119], 0
	v_mov_b32_e32 v158, 0
	v_mfma_f32_16x16x32_f16 v[128:131], v[56:59], v[116:119], 0
	v_mfma_f32_16x16x32_f16 v[132:135], v[60:63], v[116:119], 0
	v_min3_i32 v160, v136, v137, v157
	v_min3_i32 v160, v138, v139, v160
	v_min3_i32 v160, v140, v141, v160
	v_min3_i32 v160, v142, v143, v160
	v_min3_i32 v160, v144, v145, v160
	v_min3_i32 v160, v146, v147, v160
	v_min3_i32 v160, v148, v149, v160
	v_min3_i32 v156, v150, v151, v160
	v_cmp_ge_i32_e32 vcc, v156, v157
	v_mfma_f32_16x16x32_f16 v[136:139], v[64:67], v[116:119], 0
	v_mfma_f32_16x16x32_f16 v[140:143], v[68:71], v[116:119], 0
	v_cndmask_b32_e32 v158, 1, v158, vcc
	v_mfma_f32_16x16x32_f16 v[144:147], v[72:75], v[116:119], 0
	v_mfma_f32_16x16x32_f16 v[148:151], v[76:79], v[116:119], 0
	v_min3_i32 v160, v120, v121, v156
	v_min3_i32 v160, v122, v123, v160
	v_min3_i32 v160, v124, v125, v160
	v_min3_i32 v160, v126, v127, v160
	v_min3_i32 v160, v128, v129, v160
	v_min3_i32 v160, v130, v131, v160
	v_min3_i32 v160, v132, v133, v160
	v_min3_i32 v157, v134, v135, v160
	v_cmp_ge_i32_e32 vcc, v157, v156
	v_mfma_f32_16x16x32_f16 v[120:123], v[80:83], v[116:119], 0
	v_mfma_f32_16x16x32_f16 v[124:127], v[84:87], v[116:119], 0
	v_cndmask_b32_e32 v158, 2, v158, vcc
	v_mfma_f32_16x16x32_f16 v[128:131], v[88:91], v[116:119], 0
	v_mfma_f32_16x16x32_f16 v[132:135], v[92:95], v[116:119], 0
	v_min3_i32 v160, v136, v137, v157
	v_min3_i32 v160, v138, v139, v160
	v_min3_i32 v160, v140, v141, v160
	v_min3_i32 v160, v142, v143, v160
	v_min3_i32 v160, v144, v145, v160
	v_min3_i32 v160, v146, v147, v160
	v_min3_i32 v160, v148, v149, v160
	v_min3_i32 v156, v150, v151, v160
	v_cmp_ge_i32_e32 vcc, v156, v157
	v_mfma_f32_16x16x32_f16 v[136:139], v[96:99], v[116:119], 0
	v_mfma_f32_16x16x32_f16 v[140:143], v[100:103], v[116:119], 0
	v_cndmask_b32_e32 v158, 3, v158, vcc
	v_mfma_f32_16x16x32_f16 v[144:147], v[104:107], v[116:119], 0
	v_mfma_f32_16x16x32_f16 v[148:151], v[108:111], v[116:119], 0
	v_min3_i32 v160, v120, v121, v156
	v_min3_i32 v160, v122, v123, v160
	v_min3_i32 v160, v124, v125, v160
	v_min3_i32 v160, v126, v127, v160
	v_min3_i32 v160, v128, v129, v160
	v_min3_i32 v160, v130, v131, v160
	v_min3_i32 v160, v132, v133, v160
	v_min3_i32 v157, v134, v135, v160
	v_cmp_ge_i32_e32 vcc, v157, v156
	s_waitcnt vmcnt(0)
	global_load_dwordx4 v[116:119], v164, s[4:5] offset:3072
	v_mfma_f32_16x16x32_f16 v[120:123], v[16:19], v[112:115], 0
	v_mfma_f32_16x16x32_f16 v[124:127], v[20:23], v[112:115], 0
	v_cndmask_b32_e32 v158, 4, v158, vcc
	v_mfma_f32_16x16x32_f16 v[128:131], v[24:27], v[112:115], 0
	v_mfma_f32_16x16x32_f16 v[132:135], v[28:31], v[112:115], 0
	v_min3_i32 v160, v136, v137, v157
	v_min3_i32 v160, v138, v139, v160
	v_min3_i32 v160, v140, v141, v160
	v_min3_i32 v160, v142, v143, v160
	v_min3_i32 v160, v144, v145, v160
	v_min3_i32 v160, v146, v147, v160
	v_min3_i32 v160, v148, v149, v160
	v_min3_i32 v156, v150, v151, v160
	v_cmp_ge_i32_e32 vcc, v156, v157
	v_mfma_f32_16x16x32_f16 v[136:139], v[32:35], v[112:115], 0
	v_mfma_f32_16x16x32_f16 v[140:143], v[36:39], v[112:115], 0
	v_cndmask_b32_e32 v158, 5, v158, vcc
	v_add_u32_e32 v162, s40, v158
	v_lshl_or_b32 v162, v162, 2, v166
	v_mov_b32_e32 v163, v156
	ds_min_u64 v167, v[162:163] offset:16512
	v_mfma_f32_16x16x32_f16 v[144:147], v[40:43], v[112:115], 0
	v_mfma_f32_16x16x32_f16 v[148:151], v[44:47], v[112:115], 0
	v_min3_i32 v160, v120, v121, s41
	v_min3_i32 v160, v122, v123, v160
	v_min3_i32 v160, v124, v125, v160
	v_min3_i32 v160, v126, v127, v160
	v_min3_i32 v160, v128, v129, v160
	v_min3_i32 v160, v130, v131, v160
	v_min3_i32 v160, v132, v133, v160
	v_min3_i32 v157, v134, v135, v160
	v_mfma_f32_16x16x32_f16 v[120:123], v[48:51], v[112:115], 0
	v_mfma_f32_16x16x32_f16 v[124:127], v[52:55], v[112:115], 0
	v_mov_b32_e32 v158, 0
	v_mfma_f32_16x16x32_f16 v[128:131], v[56:59], v[112:115], 0
	v_mfma_f32_16x16x32_f16 v[132:135], v[60:63], v[112:115], 0
	v_min3_i32 v160, v136, v137, v157
	v_min3_i32 v160, v138, v139, v160
	v_min3_i32 v160, v140, v141, v160
	v_min3_i32 v160, v142, v143, v160
	v_min3_i32 v160, v144, v145, v160
	v_min3_i32 v160, v146, v147, v160
	v_min3_i32 v160, v148, v149, v160
	v_min3_i32 v156, v150, v151, v160
	v_cmp_ge_i32_e32 vcc, v156, v157
	v_mfma_f32_16x16x32_f16 v[136:139], v[64:67], v[112:115], 0
	v_mfma_f32_16x16x32_f16 v[140:143], v[68:71], v[112:115], 0
	v_cndmask_b32_e32 v158, 1, v158, vcc
	v_mfma_f32_16x16x32_f16 v[144:147], v[72:75], v[112:115], 0
	v_mfma_f32_16x16x32_f16 v[148:151], v[76:79], v[112:115], 0
	v_min3_i32 v160, v120, v121, v156
	v_min3_i32 v160, v122, v123, v160
	v_min3_i32 v160, v124, v125, v160
	v_min3_i32 v160, v126, v127, v160
	v_min3_i32 v160, v128, v129, v160
	v_min3_i32 v160, v130, v131, v160
	v_min3_i32 v160, v132, v133, v160
	v_min3_i32 v157, v134, v135, v160
	v_cmp_ge_i32_e32 vcc, v157, v156
	v_mfma_f32_16x16x32_f16 v[120:123], v[80:83], v[112:115], 0
	v_mfma_f32_16x16x32_f16 v[124:127], v[84:87], v[112:115], 0
	v_cndmask_b32_e32 v158, 2, v158, vcc
	v_mfma_f32_16x16x32_f16 v[128:131], v[88:91], v[112:115], 0
	v_mfma_f32_16x16x32_f16 v[132:135], v[92:95], v[112:115], 0
	v_min3_i32 v160, v136, v137, v157
	v_min3_i32 v160, v138, v139, v160
	v_min3_i32 v160, v140, v141, v160
	v_min3_i32 v160, v142, v143, v160
	v_min3_i32 v160, v144, v145, v160
	v_min3_i32 v160, v146, v147, v160
	v_min3_i32 v160, v148, v149, v160
	v_min3_i32 v156, v150, v151, v160
	v_cmp_ge_i32_e32 vcc, v156, v157
	v_mfma_f32_16x16x32_f16 v[136:139], v[96:99], v[112:115], 0
	v_mfma_f32_16x16x32_f16 v[140:143], v[100:103], v[112:115], 0
	v_cndmask_b32_e32 v158, 3, v158, vcc
	v_mfma_f32_16x16x32_f16 v[144:147], v[104:107], v[112:115], 0
	v_mfma_f32_16x16x32_f16 v[148:151], v[108:111], v[112:115], 0
	v_min3_i32 v160, v120, v121, v156
	v_min3_i32 v160, v122, v123, v160
	v_min3_i32 v160, v124, v125, v160
	v_min3_i32 v160, v126, v127, v160
	v_min3_i32 v160, v128, v129, v160
	v_min3_i32 v160, v130, v131, v160
	v_min3_i32 v160, v132, v133, v160
	v_min3_i32 v157, v134, v135, v160
	v_cmp_ge_i32_e32 vcc, v157, v156
	s_waitcnt vmcnt(0)
	global_load_dwordx4 v[112:115], v164, s[22:23]
	v_mfma_f32_16x16x32_f16 v[120:123], v[16:19], v[116:119], 0
	v_mfma_f32_16x16x32_f16 v[124:127], v[20:23], v[116:119], 0
	v_cndmask_b32_e32 v158, 4, v158, vcc
	v_mfma_f32_16x16x32_f16 v[128:131], v[24:27], v[116:119], 0
	v_mfma_f32_16x16x32_f16 v[132:135], v[28:31], v[116:119], 0
	v_min3_i32 v160, v136, v137, v157
	v_min3_i32 v160, v138, v139, v160
	v_min3_i32 v160, v140, v141, v160
	v_min3_i32 v160, v142, v143, v160
	v_min3_i32 v160, v144, v145, v160
	v_min3_i32 v160, v146, v147, v160
	v_min3_i32 v160, v148, v149, v160
	v_min3_i32 v156, v150, v151, v160
	v_cmp_ge_i32_e32 vcc, v156, v157
	v_mfma_f32_16x16x32_f16 v[136:139], v[32:35], v[116:119], 0
	v_mfma_f32_16x16x32_f16 v[140:143], v[36:39], v[116:119], 0
	v_cndmask_b32_e32 v158, 5, v158, vcc
	v_add_u32_e32 v162, s40, v158
	v_lshl_or_b32 v162, v162, 2, v166
	v_mov_b32_e32 v163, v156
	ds_min_u64 v167, v[162:163] offset:16640
	v_mfma_f32_16x16x32_f16 v[144:147], v[40:43], v[116:119], 0
	v_mfma_f32_16x16x32_f16 v[148:151], v[44:47], v[116:119], 0
	v_min3_i32 v160, v120, v121, s41
	v_min3_i32 v160, v122, v123, v160
	v_min3_i32 v160, v124, v125, v160
	v_min3_i32 v160, v126, v127, v160
	v_min3_i32 v160, v128, v129, v160
	v_min3_i32 v160, v130, v131, v160
	v_min3_i32 v160, v132, v133, v160
	v_min3_i32 v157, v134, v135, v160
	v_mfma_f32_16x16x32_f16 v[120:123], v[48:51], v[116:119], 0
	v_mfma_f32_16x16x32_f16 v[124:127], v[52:55], v[116:119], 0
	v_mov_b32_e32 v158, 0
	v_mfma_f32_16x16x32_f16 v[128:131], v[56:59], v[116:119], 0
	v_mfma_f32_16x16x32_f16 v[132:135], v[60:63], v[116:119], 0
	v_min3_i32 v160, v136, v137, v157
	v_min3_i32 v160, v138, v139, v160
	v_min3_i32 v160, v140, v141, v160
	v_min3_i32 v160, v142, v143, v160
	v_min3_i32 v160, v144, v145, v160
	v_min3_i32 v160, v146, v147, v160
	v_min3_i32 v160, v148, v149, v160
	v_min3_i32 v156, v150, v151, v160
	v_cmp_ge_i32_e32 vcc, v156, v157
	v_mfma_f32_16x16x32_f16 v[136:139], v[64:67], v[116:119], 0
	v_mfma_f32_16x16x32_f16 v[140:143], v[68:71], v[116:119], 0
	v_cndmask_b32_e32 v158, 1, v158, vcc
	v_mfma_f32_16x16x32_f16 v[144:147], v[72:75], v[116:119], 0
	v_mfma_f32_16x16x32_f16 v[148:151], v[76:79], v[116:119], 0
	v_min3_i32 v160, v120, v121, v156
	v_min3_i32 v160, v122, v123, v160
	v_min3_i32 v160, v124, v125, v160
	v_min3_i32 v160, v126, v127, v160
	v_min3_i32 v160, v128, v129, v160
	v_min3_i32 v160, v130, v131, v160
	v_min3_i32 v160, v132, v133, v160
	v_min3_i32 v157, v134, v135, v160
	v_cmp_ge_i32_e32 vcc, v157, v156
	v_mfma_f32_16x16x32_f16 v[120:123], v[80:83], v[116:119], 0
	v_mfma_f32_16x16x32_f16 v[124:127], v[84:87], v[116:119], 0
	v_cndmask_b32_e32 v158, 2, v158, vcc
	v_mfma_f32_16x16x32_f16 v[128:131], v[88:91], v[116:119], 0
	v_mfma_f32_16x16x32_f16 v[132:135], v[92:95], v[116:119], 0
	v_min3_i32 v160, v136, v137, v157
	v_min3_i32 v160, v138, v139, v160
	v_min3_i32 v160, v140, v141, v160
	v_min3_i32 v160, v142, v143, v160
	v_min3_i32 v160, v144, v145, v160
	v_min3_i32 v160, v146, v147, v160
	v_min3_i32 v160, v148, v149, v160
	v_min3_i32 v156, v150, v151, v160
	v_cmp_ge_i32_e32 vcc, v156, v157
	v_mfma_f32_16x16x32_f16 v[136:139], v[96:99], v[116:119], 0
	v_mfma_f32_16x16x32_f16 v[140:143], v[100:103], v[116:119], 0
	v_cndmask_b32_e32 v158, 3, v158, vcc
	v_mfma_f32_16x16x32_f16 v[144:147], v[104:107], v[116:119], 0
	v_mfma_f32_16x16x32_f16 v[148:151], v[108:111], v[116:119], 0
	v_min3_i32 v160, v120, v121, v156
	v_min3_i32 v160, v122, v123, v160
	v_min3_i32 v160, v124, v125, v160
	v_min3_i32 v160, v126, v127, v160
	v_min3_i32 v160, v128, v129, v160
	v_min3_i32 v160, v130, v131, v160
	v_min3_i32 v160, v132, v133, v160
	v_min3_i32 v157, v134, v135, v160
	v_cmp_ge_i32_e32 vcc, v157, v156
	s_waitcnt vmcnt(0)
	global_load_dwordx4 v[116:119], v164, s[22:23] offset:1024
	v_mfma_f32_16x16x32_f16 v[120:123], v[16:19], v[112:115], 0
	v_mfma_f32_16x16x32_f16 v[124:127], v[20:23], v[112:115], 0
	v_cndmask_b32_e32 v158, 4, v158, vcc
	v_mfma_f32_16x16x32_f16 v[128:131], v[24:27], v[112:115], 0
	v_mfma_f32_16x16x32_f16 v[132:135], v[28:31], v[112:115], 0
	v_min3_i32 v160, v136, v137, v157
	v_min3_i32 v160, v138, v139, v160
	v_min3_i32 v160, v140, v141, v160
	v_min3_i32 v160, v142, v143, v160
	v_min3_i32 v160, v144, v145, v160
	v_min3_i32 v160, v146, v147, v160
	v_min3_i32 v160, v148, v149, v160
	v_min3_i32 v156, v150, v151, v160
	v_cmp_ge_i32_e32 vcc, v156, v157
	v_mfma_f32_16x16x32_f16 v[136:139], v[32:35], v[112:115], 0
	v_mfma_f32_16x16x32_f16 v[140:143], v[36:39], v[112:115], 0
	v_cndmask_b32_e32 v158, 5, v158, vcc
	v_add_u32_e32 v162, s40, v158
	v_lshl_or_b32 v162, v162, 2, v166
	v_mov_b32_e32 v163, v156
	ds_min_u64 v167, v[162:163] offset:16768
	v_mfma_f32_16x16x32_f16 v[144:147], v[40:43], v[112:115], 0
	v_mfma_f32_16x16x32_f16 v[148:151], v[44:47], v[112:115], 0
	v_min3_i32 v160, v120, v121, s41
	v_min3_i32 v160, v122, v123, v160
	v_min3_i32 v160, v124, v125, v160
	v_min3_i32 v160, v126, v127, v160
	v_min3_i32 v160, v128, v129, v160
	v_min3_i32 v160, v130, v131, v160
	v_min3_i32 v160, v132, v133, v160
	v_min3_i32 v157, v134, v135, v160
	v_mfma_f32_16x16x32_f16 v[120:123], v[48:51], v[112:115], 0
	v_mfma_f32_16x16x32_f16 v[124:127], v[52:55], v[112:115], 0
	v_mov_b32_e32 v158, 0
	v_mfma_f32_16x16x32_f16 v[128:131], v[56:59], v[112:115], 0
	v_mfma_f32_16x16x32_f16 v[132:135], v[60:63], v[112:115], 0
	v_min3_i32 v160, v136, v137, v157
	v_min3_i32 v160, v138, v139, v160
	v_min3_i32 v160, v140, v141, v160
	v_min3_i32 v160, v142, v143, v160
	v_min3_i32 v160, v144, v145, v160
	v_min3_i32 v160, v146, v147, v160
	v_min3_i32 v160, v148, v149, v160
	v_min3_i32 v156, v150, v151, v160
	v_cmp_ge_i32_e32 vcc, v156, v157
	v_mfma_f32_16x16x32_f16 v[136:139], v[64:67], v[112:115], 0
	v_mfma_f32_16x16x32_f16 v[140:143], v[68:71], v[112:115], 0
	v_cndmask_b32_e32 v158, 1, v158, vcc
	v_mfma_f32_16x16x32_f16 v[144:147], v[72:75], v[112:115], 0
	v_mfma_f32_16x16x32_f16 v[148:151], v[76:79], v[112:115], 0
	v_min3_i32 v160, v120, v121, v156
	v_min3_i32 v160, v122, v123, v160
	v_min3_i32 v160, v124, v125, v160
	v_min3_i32 v160, v126, v127, v160
	v_min3_i32 v160, v128, v129, v160
	v_min3_i32 v160, v130, v131, v160
	v_min3_i32 v160, v132, v133, v160
	v_min3_i32 v157, v134, v135, v160
	v_cmp_ge_i32_e32 vcc, v157, v156
	v_mfma_f32_16x16x32_f16 v[120:123], v[80:83], v[112:115], 0
	v_mfma_f32_16x16x32_f16 v[124:127], v[84:87], v[112:115], 0
	v_cndmask_b32_e32 v158, 2, v158, vcc
	v_mfma_f32_16x16x32_f16 v[128:131], v[88:91], v[112:115], 0
	v_mfma_f32_16x16x32_f16 v[132:135], v[92:95], v[112:115], 0
	v_min3_i32 v160, v136, v137, v157
	v_min3_i32 v160, v138, v139, v160
	v_min3_i32 v160, v140, v141, v160
	v_min3_i32 v160, v142, v143, v160
	v_min3_i32 v160, v144, v145, v160
	v_min3_i32 v160, v146, v147, v160
	v_min3_i32 v160, v148, v149, v160
	v_min3_i32 v156, v150, v151, v160
	v_cmp_ge_i32_e32 vcc, v156, v157
	v_mfma_f32_16x16x32_f16 v[136:139], v[96:99], v[112:115], 0
	v_mfma_f32_16x16x32_f16 v[140:143], v[100:103], v[112:115], 0
	v_cndmask_b32_e32 v158, 3, v158, vcc
	v_mfma_f32_16x16x32_f16 v[144:147], v[104:107], v[112:115], 0
	v_mfma_f32_16x16x32_f16 v[148:151], v[108:111], v[112:115], 0
	v_min3_i32 v160, v120, v121, v156
	v_min3_i32 v160, v122, v123, v160
	v_min3_i32 v160, v124, v125, v160
	v_min3_i32 v160, v126, v127, v160
	v_min3_i32 v160, v128, v129, v160
	v_min3_i32 v160, v130, v131, v160
	v_min3_i32 v160, v132, v133, v160
	v_min3_i32 v157, v134, v135, v160
	v_cmp_ge_i32_e32 vcc, v157, v156
	s_waitcnt vmcnt(0)
	global_load_dwordx4 v[112:115], v164, s[22:23] offset:2048
	v_mfma_f32_16x16x32_f16 v[120:123], v[16:19], v[116:119], 0
	v_mfma_f32_16x16x32_f16 v[124:127], v[20:23], v[116:119], 0
	v_cndmask_b32_e32 v158, 4, v158, vcc
	v_mfma_f32_16x16x32_f16 v[128:131], v[24:27], v[116:119], 0
	v_mfma_f32_16x16x32_f16 v[132:135], v[28:31], v[116:119], 0
	v_min3_i32 v160, v136, v137, v157
	v_min3_i32 v160, v138, v139, v160
	v_min3_i32 v160, v140, v141, v160
	v_min3_i32 v160, v142, v143, v160
	v_min3_i32 v160, v144, v145, v160
	v_min3_i32 v160, v146, v147, v160
	v_min3_i32 v160, v148, v149, v160
	v_min3_i32 v156, v150, v151, v160
	v_cmp_ge_i32_e32 vcc, v156, v157
	v_mfma_f32_16x16x32_f16 v[136:139], v[32:35], v[116:119], 0
	v_mfma_f32_16x16x32_f16 v[140:143], v[36:39], v[116:119], 0
	v_cndmask_b32_e32 v158, 5, v158, vcc
	v_add_u32_e32 v162, s40, v158
	v_lshl_or_b32 v162, v162, 2, v166
	v_mov_b32_e32 v163, v156
	ds_min_u64 v167, v[162:163] offset:16896
	v_mfma_f32_16x16x32_f16 v[144:147], v[40:43], v[116:119], 0
	v_mfma_f32_16x16x32_f16 v[148:151], v[44:47], v[116:119], 0
	v_min3_i32 v160, v120, v121, s41
	v_min3_i32 v160, v122, v123, v160
	v_min3_i32 v160, v124, v125, v160
	v_min3_i32 v160, v126, v127, v160
	v_min3_i32 v160, v128, v129, v160
	v_min3_i32 v160, v130, v131, v160
	v_min3_i32 v160, v132, v133, v160
	v_min3_i32 v157, v134, v135, v160
	v_mfma_f32_16x16x32_f16 v[120:123], v[48:51], v[116:119], 0
	v_mfma_f32_16x16x32_f16 v[124:127], v[52:55], v[116:119], 0
	v_mov_b32_e32 v158, 0
	v_mfma_f32_16x16x32_f16 v[128:131], v[56:59], v[116:119], 0
	v_mfma_f32_16x16x32_f16 v[132:135], v[60:63], v[116:119], 0
	v_min3_i32 v160, v136, v137, v157
	v_min3_i32 v160, v138, v139, v160
	v_min3_i32 v160, v140, v141, v160
	v_min3_i32 v160, v142, v143, v160
	v_min3_i32 v160, v144, v145, v160
	v_min3_i32 v160, v146, v147, v160
	v_min3_i32 v160, v148, v149, v160
	v_min3_i32 v156, v150, v151, v160
	v_cmp_ge_i32_e32 vcc, v156, v157
	v_mfma_f32_16x16x32_f16 v[136:139], v[64:67], v[116:119], 0
	v_mfma_f32_16x16x32_f16 v[140:143], v[68:71], v[116:119], 0
	v_cndmask_b32_e32 v158, 1, v158, vcc
	v_mfma_f32_16x16x32_f16 v[144:147], v[72:75], v[116:119], 0
	v_mfma_f32_16x16x32_f16 v[148:151], v[76:79], v[116:119], 0
	v_min3_i32 v160, v120, v121, v156
	v_min3_i32 v160, v122, v123, v160
	v_min3_i32 v160, v124, v125, v160
	v_min3_i32 v160, v126, v127, v160
	v_min3_i32 v160, v128, v129, v160
	v_min3_i32 v160, v130, v131, v160
	v_min3_i32 v160, v132, v133, v160
	v_min3_i32 v157, v134, v135, v160
	v_cmp_ge_i32_e32 vcc, v157, v156
	v_mfma_f32_16x16x32_f16 v[120:123], v[80:83], v[116:119], 0
	v_mfma_f32_16x16x32_f16 v[124:127], v[84:87], v[116:119], 0
	v_cndmask_b32_e32 v158, 2, v158, vcc
	v_mfma_f32_16x16x32_f16 v[128:131], v[88:91], v[116:119], 0
	v_mfma_f32_16x16x32_f16 v[132:135], v[92:95], v[116:119], 0
	v_min3_i32 v160, v136, v137, v157
	v_min3_i32 v160, v138, v139, v160
	v_min3_i32 v160, v140, v141, v160
	v_min3_i32 v160, v142, v143, v160
	v_min3_i32 v160, v144, v145, v160
	v_min3_i32 v160, v146, v147, v160
	v_min3_i32 v160, v148, v149, v160
	v_min3_i32 v156, v150, v151, v160
	v_cmp_ge_i32_e32 vcc, v156, v157
	v_mfma_f32_16x16x32_f16 v[136:139], v[96:99], v[116:119], 0
	v_mfma_f32_16x16x32_f16 v[140:143], v[100:103], v[116:119], 0
	v_cndmask_b32_e32 v158, 3, v158, vcc
	v_mfma_f32_16x16x32_f16 v[144:147], v[104:107], v[116:119], 0
	v_mfma_f32_16x16x32_f16 v[148:151], v[108:111], v[116:119], 0
	v_min3_i32 v160, v120, v121, v156
	v_min3_i32 v160, v122, v123, v160
	v_min3_i32 v160, v124, v125, v160
	v_min3_i32 v160, v126, v127, v160
	v_min3_i32 v160, v128, v129, v160
	v_min3_i32 v160, v130, v131, v160
	v_min3_i32 v160, v132, v133, v160
	v_min3_i32 v157, v134, v135, v160
	v_cmp_ge_i32_e32 vcc, v157, v156
	s_waitcnt vmcnt(0)
	global_load_dwordx4 v[116:119], v164, s[22:23] offset:3072
	v_mfma_f32_16x16x32_f16 v[120:123], v[16:19], v[112:115], 0
	v_mfma_f32_16x16x32_f16 v[124:127], v[20:23], v[112:115], 0
	v_cndmask_b32_e32 v158, 4, v158, vcc
	v_mfma_f32_16x16x32_f16 v[128:131], v[24:27], v[112:115], 0
	v_mfma_f32_16x16x32_f16 v[132:135], v[28:31], v[112:115], 0
	v_min3_i32 v160, v136, v137, v157
	v_min3_i32 v160, v138, v139, v160
	v_min3_i32 v160, v140, v141, v160
	v_min3_i32 v160, v142, v143, v160
	v_min3_i32 v160, v144, v145, v160
	v_min3_i32 v160, v146, v147, v160
	v_min3_i32 v160, v148, v149, v160
	v_min3_i32 v156, v150, v151, v160
	v_cmp_ge_i32_e32 vcc, v156, v157
	v_mfma_f32_16x16x32_f16 v[136:139], v[32:35], v[112:115], 0
	v_mfma_f32_16x16x32_f16 v[140:143], v[36:39], v[112:115], 0
	v_cndmask_b32_e32 v158, 5, v158, vcc
	v_add_u32_e32 v162, s40, v158
	v_lshl_or_b32 v162, v162, 2, v166
	v_mov_b32_e32 v163, v156
	ds_min_u64 v167, v[162:163] offset:17024
	v_mfma_f32_16x16x32_f16 v[144:147], v[40:43], v[112:115], 0
	v_mfma_f32_16x16x32_f16 v[148:151], v[44:47], v[112:115], 0
	v_min3_i32 v160, v120, v121, s41
	v_min3_i32 v160, v122, v123, v160
	v_min3_i32 v160, v124, v125, v160
	v_min3_i32 v160, v126, v127, v160
	v_min3_i32 v160, v128, v129, v160
	v_min3_i32 v160, v130, v131, v160
	v_min3_i32 v160, v132, v133, v160
	v_min3_i32 v157, v134, v135, v160
	s_waitcnt lgkmcnt(0)
	s_barrier
	s_lshl_b32 s60, s50, 7
	v_add_u32_e32 v2, s60, v169
	ds_read_b32 v178, v2 offset:16384
	s_lshl_b32 s60, s50, 10
	v_add_u32_e32 v210, s60, v170
	s_cmp_lt_u32 s50, 2
	s_cbranch_scc0 .Lp1a_y
	s_add_i32 s65, s50, 4
	s_lshl_b32 s60, s65, 7
	v_add_u32_e32 v2, s60, v169
	ds_read_b32 v216, v2 offset:16384
	s_lshl_b32 s60, s65, 10
	v_add_u32_e32 v248, s60, v170
